# P12 epilogue: 16 x-loads per row-half issued together, counted vmcnt instead of 32 serialized round trips
# baseline (speedup 1.0000x reference)
.LBB0_2448:
	v_lshl_add_u32 v26, s46, 8, v1
	v_lshl_or_b32 v20, s36, 8, v183
	v_ashrrev_i32_e32 v27, 31, v26
	v_ashrrev_i32_e32 v21, 31, v20
	v_lshlrev_b64 v[2:3], 12, v[26:27]
	v_readlane_b32 s36, v254, 19
	v_lshl_add_u64 v[18:19], v[2:3], 0, v[20:21]
	v_readlane_b32 s37, v254, 20
	v_lshl_add_u64 v[2:3], v[20:21], 2, s[10:11]
	v_lshl_add_u64 v[30:31], v[18:19], 1, s[8:9]
	v_lshl_add_u64 v[28:29], v[18:19], 2, s[36:37]
	global_load_dwordx4 v[14:17], v[2:3], off
	global_load_dwordx4 v[10:13], v[2:3], off offset:64
	global_load_dwordx4 v[6:9], v[2:3], off offset:512
	s_nop 0
	global_load_dwordx4 v[2:5], v[2:3], off offset:576
	s_mov_b32 s98, 0x40000
	s_mov_b32 s99, 0
	v_mov_b32_e32 v178, v28
	v_mov_b32_e32 v179, v29
	global_load_dwordx4 v[190:193], v[178:179], off
	global_load_dwordx4 v[194:197], v[178:179], off offset:64
	global_load_dwordx4 v[198:201], v[178:179], off offset:512
	global_load_dwordx4 v[202:205], v[178:179], off offset:576
	v_lshl_add_u64 v[178:179], v[178:179], 0, s[98:99]
	global_load_dwordx4 v[206:209], v[178:179], off
	global_load_dwordx4 v[210:213], v[178:179], off offset:64
	global_load_dwordx4 v[214:217], v[178:179], off offset:512
	global_load_dwordx4 v[218:221], v[178:179], off offset:576
	v_lshl_add_u64 v[178:179], v[178:179], 0, s[98:99]
	global_load_dwordx4 v[222:225], v[178:179], off
	global_load_dwordx4 v[226:229], v[178:179], off offset:64
	global_load_dwordx4 v[230:233], v[178:179], off offset:512
	global_load_dwordx4 v[234:237], v[178:179], off offset:576
	v_lshl_add_u64 v[178:179], v[178:179], 0, s[98:99]
	global_load_dwordx4 v[238:241], v[178:179], off
	global_load_dwordx4 v[242:245], v[178:179], off offset:64
	global_load_dwordx4 v[246:249], v[178:179], off offset:512
	global_load_dwordx4 v[250:253], v[178:179], off offset:576
	s_andn2_b64 vcc, exec, s[0:1]
	s_mov_b64 s[0:1], -1
	v_readlane_b32 s38, v254, 21
	v_readlane_b32 s39, v254, 22
	v_readlane_b32 s40, v254, 23
	v_readlane_b32 s41, v254, 24
	v_readlane_b32 s42, v254, 25
	v_readlane_b32 s43, v254, 26
	v_readlane_b32 s44, v254, 27
	v_readlane_b32 s45, v254, 28
	v_readlane_b32 s46, v254, 29
	v_readlane_b32 s47, v254, 30
	v_readlane_b32 s48, v254, 31
	v_readlane_b32 s49, v254, 32
	v_readlane_b32 s50, v254, 33
	v_readlane_b32 s51, v254, 34
	s_waitcnt vmcnt(15)
	v_pk_mul_f32 v[192:193], v[192:193], s[16:17] op_sel_hi:[1,0]
	v_pk_mul_f32 v[190:191], v[190:191], s[16:17] op_sel_hi:[1,0]
	v_pk_fma_f32 v[192:193], v[160:161], v[16:17], v[192:193]
	v_pk_fma_f32 v[190:191], v[158:159], v[14:15], v[190:191]
	s_nop 0
	v_cvt_pk_bf16_f32 v190, v190, v191
	v_cvt_pk_bf16_f32 v191, v192, v193
	global_store_dwordx2 v[30:31], v[190:191], off
	s_waitcnt vmcnt(15)
	v_pk_mul_f32 v[196:197], v[196:197], s[16:17] op_sel_hi:[1,0]
	v_pk_mul_f32 v[194:195], v[194:195], s[16:17] op_sel_hi:[1,0]
	v_pk_fma_f32 v[196:197], v[156:157], v[12:13], v[196:197]
	v_pk_fma_f32 v[194:195], v[154:155], v[10:11], v[194:195]
	s_nop 0
	v_cvt_pk_bf16_f32 v194, v194, v195
	v_cvt_pk_bf16_f32 v195, v196, v197
	global_store_dwordx2 v[30:31], v[194:195], off offset:32
	s_waitcnt vmcnt(15)
	v_pk_mul_f32 v[200:201], v[200:201], s[16:17] op_sel_hi:[1,0]
	v_pk_mul_f32 v[198:199], v[198:199], s[16:17] op_sel_hi:[1,0]
	v_pk_fma_f32 v[200:201], v[152:153], v[8:9], v[200:201]
	v_pk_fma_f32 v[198:199], v[150:151], v[6:7], v[198:199]
	s_nop 0
	v_cvt_pk_bf16_f32 v198, v198, v199
	v_cvt_pk_bf16_f32 v199, v200, v201
	global_store_dwordx2 v[30:31], v[198:199], off offset:256
	v_or_b32_e32 v28, 16, v26
	v_ashrrev_i32_e32 v29, 31, v28
	v_lshlrev_b64 v[28:29], 12, v[28:29]
	v_lshl_add_u64 v[28:29], v[28:29], 0, v[20:21]
	v_lshl_add_u64 v[32:33], v[28:29], 2, s[36:37]
	v_lshl_add_u64 v[28:29], v[28:29], 1, s[8:9]
	s_waitcnt vmcnt(15)
	v_pk_mul_f32 v[204:205], v[204:205], s[16:17] op_sel_hi:[1,0]
	v_pk_mul_f32 v[202:203], v[202:203], s[16:17] op_sel_hi:[1,0]
	v_pk_fma_f32 v[204:205], v[144:145], v[4:5], v[204:205]
	v_pk_fma_f32 v[202:203], v[142:143], v[2:3], v[202:203]
	s_nop 0
	v_cvt_pk_bf16_f32 v202, v202, v203
	v_cvt_pk_bf16_f32 v203, v204, v205
	global_store_dwordx2 v[30:31], v[202:203], off offset:288
	v_or_b32_e32 v30, 32, v26
	v_ashrrev_i32_e32 v31, 31, v30
	v_lshlrev_b64 v[30:31], 12, v[30:31]
	v_lshl_add_u64 v[30:31], v[30:31], 0, v[20:21]
	v_or_b32_e32 v26, 48, v26
	v_ashrrev_i32_e32 v27, 31, v26
	v_lshlrev_b64 v[26:27], 12, v[26:27]
	v_lshl_add_u64 v[26:27], v[26:27], 0, v[20:21]
	s_waitcnt vmcnt(15)
	v_pk_mul_f32 v[208:209], v[208:209], s[16:17] op_sel_hi:[1,0]
	v_pk_mul_f32 v[206:207], v[206:207], s[16:17] op_sel_hi:[1,0]
	v_pk_fma_f32 v[208:209], v[148:149], v[16:17], v[208:209]
	v_pk_fma_f32 v[206:207], v[146:147], v[14:15], v[206:207]
	s_nop 0
	v_cvt_pk_bf16_f32 v206, v206, v207
	v_cvt_pk_bf16_f32 v207, v208, v209
	global_store_dwordx2 v[28:29], v[206:207], off
	s_waitcnt vmcnt(15)
	v_pk_mul_f32 v[212:213], v[212:213], s[16:17] op_sel_hi:[1,0]
	v_pk_mul_f32 v[210:211], v[210:211], s[16:17] op_sel_hi:[1,0]
	v_pk_fma_f32 v[212:213], v[140:141], v[12:13], v[212:213]
	v_pk_fma_f32 v[210:211], v[138:139], v[10:11], v[210:211]
	s_nop 0
	v_cvt_pk_bf16_f32 v210, v210, v211
	v_cvt_pk_bf16_f32 v211, v212, v213
	global_store_dwordx2 v[28:29], v[210:211], off offset:32
	s_waitcnt vmcnt(15)
	v_pk_mul_f32 v[216:217], v[216:217], s[16:17] op_sel_hi:[1,0]
	v_pk_mul_f32 v[214:215], v[214:215], s[16:17] op_sel_hi:[1,0]
	v_pk_fma_f32 v[216:217], v[136:137], v[8:9], v[216:217]
	v_pk_fma_f32 v[214:215], v[134:135], v[6:7], v[214:215]
	s_nop 0
	v_cvt_pk_bf16_f32 v214, v214, v215
	v_cvt_pk_bf16_f32 v215, v216, v217
	global_store_dwordx2 v[28:29], v[214:215], off offset:256
	v_lshl_add_u64 v[32:33], v[30:31], 2, s[36:37]
	s_waitcnt vmcnt(15)
	v_pk_mul_f32 v[220:221], v[220:221], s[16:17] op_sel_hi:[1,0]
	v_pk_mul_f32 v[218:219], v[218:219], s[16:17] op_sel_hi:[1,0]
	v_pk_fma_f32 v[220:221], v[128:129], v[4:5], v[220:221]
	v_pk_fma_f32 v[218:219], v[126:127], v[2:3], v[218:219]
	s_nop 0
	v_cvt_pk_bf16_f32 v218, v218, v219
	v_cvt_pk_bf16_f32 v219, v220, v221
	global_store_dwordx2 v[28:29], v[218:219], off offset:288
	v_lshl_add_u64 v[28:29], v[30:31], 1, s[8:9]
	v_lshl_add_u64 v[30:31], v[26:27], 2, s[36:37]
	s_waitcnt vmcnt(15)
	v_pk_mul_f32 v[224:225], v[224:225], s[16:17] op_sel_hi:[1,0]
	v_pk_mul_f32 v[222:223], v[222:223], s[16:17] op_sel_hi:[1,0]
	v_pk_fma_f32 v[224:225], v[132:133], v[16:17], v[224:225]
	v_pk_fma_f32 v[222:223], v[130:131], v[14:15], v[222:223]
	s_nop 0
	v_cvt_pk_bf16_f32 v222, v222, v223
	v_cvt_pk_bf16_f32 v223, v224, v225
	global_store_dwordx2 v[28:29], v[222:223], off
	s_waitcnt vmcnt(15)
	v_pk_mul_f32 v[228:229], v[228:229], s[16:17] op_sel_hi:[1,0]
	v_pk_mul_f32 v[226:227], v[226:227], s[16:17] op_sel_hi:[1,0]
	v_pk_fma_f32 v[228:229], v[124:125], v[12:13], v[228:229]
	v_pk_fma_f32 v[226:227], v[122:123], v[10:11], v[226:227]
	s_nop 0
	v_cvt_pk_bf16_f32 v226, v226, v227
	v_cvt_pk_bf16_f32 v227, v228, v229
	global_store_dwordx2 v[28:29], v[226:227], off offset:32
	s_waitcnt vmcnt(15)
	v_pk_mul_f32 v[232:233], v[232:233], s[16:17] op_sel_hi:[1,0]
	v_pk_mul_f32 v[230:231], v[230:231], s[16:17] op_sel_hi:[1,0]
	v_pk_fma_f32 v[232:233], v[120:121], v[8:9], v[232:233]
	v_pk_fma_f32 v[230:231], v[118:119], v[6:7], v[230:231]
	s_nop 0
	v_cvt_pk_bf16_f32 v230, v230, v231
	v_cvt_pk_bf16_f32 v231, v232, v233
	global_store_dwordx2 v[28:29], v[230:231], off offset:256
	s_waitcnt vmcnt(15)
	v_pk_mul_f32 v[20:21], v[236:237], s[16:17] op_sel_hi:[1,0]
	v_pk_mul_f32 v[234:235], v[234:235], s[16:17] op_sel_hi:[1,0]
	v_pk_fma_f32 v[20:21], v[112:113], v[4:5], v[20:21]
	v_pk_fma_f32 v[234:235], v[110:111], v[2:3], v[234:235]
	v_lshl_add_u64 v[24:25], v[26:27], 1, s[8:9]
	v_cvt_pk_bf16_f32 v234, v234, v235
	v_cvt_pk_bf16_f32 v235, v20, v21
	global_store_dwordx2 v[28:29], v[234:235], off offset:288
	v_lshl_add_u64 v[26:27], v[18:19], 0, s[4:5]
	v_lshl_add_u64 v[28:29], v[26:27], 2, s[36:37]
	s_waitcnt vmcnt(15)
	v_pk_mul_f32 v[240:241], v[240:241], s[16:17] op_sel_hi:[1,0]
	v_pk_mul_f32 v[238:239], v[238:239], s[16:17] op_sel_hi:[1,0]
	v_pk_fma_f32 v[240:241], v[116:117], v[16:17], v[240:241]
	v_pk_fma_f32 v[238:239], v[114:115], v[14:15], v[238:239]
	s_nop 0
	v_cvt_pk_bf16_f32 v238, v238, v239
	v_cvt_pk_bf16_f32 v239, v240, v241
	global_store_dwordx2 v[24:25], v[238:239], off
	s_waitcnt vmcnt(15)
	v_pk_mul_f32 v[244:245], v[244:245], s[16:17] op_sel_hi:[1,0]
	v_pk_mul_f32 v[242:243], v[242:243], s[16:17] op_sel_hi:[1,0]
	v_pk_fma_f32 v[244:245], v[108:109], v[12:13], v[244:245]
	v_pk_fma_f32 v[242:243], v[106:107], v[10:11], v[242:243]
	s_nop 0
	v_cvt_pk_bf16_f32 v242, v242, v243
	v_cvt_pk_bf16_f32 v243, v244, v245
	global_store_dwordx2 v[24:25], v[242:243], off offset:32
	s_waitcnt vmcnt(15)
	v_pk_mul_f32 v[248:249], v[248:249], s[16:17] op_sel_hi:[1,0]
	v_pk_mul_f32 v[246:247], v[246:247], s[16:17] op_sel_hi:[1,0]
	v_pk_fma_f32 v[248:249], v[104:105], v[8:9], v[248:249]
	v_pk_fma_f32 v[246:247], v[102:103], v[6:7], v[246:247]
	s_nop 0
	v_cvt_pk_bf16_f32 v246, v246, v247
	v_cvt_pk_bf16_f32 v247, v248, v249
	global_store_dwordx2 v[24:25], v[246:247], off offset:256
	s_waitcnt vmcnt(15)
	v_pk_mul_f32 v[252:253], v[252:253], s[16:17] op_sel_hi:[1,0]
	v_pk_mul_f32 v[250:251], v[250:251], s[16:17] op_sel_hi:[1,0]
	v_pk_fma_f32 v[252:253], v[100:101], v[4:5], v[252:253]
	v_pk_fma_f32 v[250:251], v[98:99], v[2:3], v[250:251]
	s_nop 0
	v_cvt_pk_bf16_f32 v250, v250, v251
	v_cvt_pk_bf16_f32 v251, v252, v253
	global_store_dwordx2 v[24:25], v[250:251], off offset:288
	v_lshl_add_u64 v[178:179], v[178:179], 0, s[98:99]
	v_lshl_add_u64 v[178:179], v[178:179], 0, s[98:99]
	v_lshl_add_u64 v[178:179], v[178:179], 0, s[98:99]
	v_lshl_add_u64 v[178:179], v[178:179], 0, s[98:99]
	v_lshl_add_u64 v[178:179], v[178:179], 0, s[98:99]
	global_load_dwordx4 v[190:193], v[178:179], off
	global_load_dwordx4 v[194:197], v[178:179], off offset:64
	global_load_dwordx4 v[198:201], v[178:179], off offset:512
	global_load_dwordx4 v[202:205], v[178:179], off offset:576
	v_lshl_add_u64 v[178:179], v[178:179], 0, s[98:99]
	global_load_dwordx4 v[206:209], v[178:179], off
	global_load_dwordx4 v[210:213], v[178:179], off offset:64
	global_load_dwordx4 v[214:217], v[178:179], off offset:512
	global_load_dwordx4 v[218:221], v[178:179], off offset:576
	v_lshl_add_u64 v[178:179], v[178:179], 0, s[98:99]
	global_load_dwordx4 v[222:225], v[178:179], off
	global_load_dwordx4 v[226:229], v[178:179], off offset:64
	global_load_dwordx4 v[230:233], v[178:179], off offset:512
	global_load_dwordx4 v[234:237], v[178:179], off offset:576
	v_lshl_add_u64 v[178:179], v[178:179], 0, s[98:99]
	global_load_dwordx4 v[238:241], v[178:179], off
	global_load_dwordx4 v[242:245], v[178:179], off offset:64
	global_load_dwordx4 v[246:249], v[178:179], off offset:512
	global_load_dwordx4 v[250:253], v[178:179], off offset:576
	v_lshl_add_u64 v[24:25], v[26:27], 1, s[8:9]
	v_lshl_add_u64 v[26:27], v[18:19], 0, s[18:19]
	s_waitcnt vmcnt(15)
	v_pk_mul_f32 v[192:193], v[192:193], s[16:17] op_sel_hi:[1,0]
	v_pk_mul_f32 v[190:191], v[190:191], s[16:17] op_sel_hi:[1,0]
	v_pk_fma_f32 v[192:193], v[96:97], v[16:17], v[192:193]
	v_pk_fma_f32 v[190:191], v[94:95], v[14:15], v[190:191]
	s_nop 0
	v_cvt_pk_bf16_f32 v190, v190, v191
	v_cvt_pk_bf16_f32 v191, v192, v193
	global_store_dwordx2 v[24:25], v[190:191], off
	s_waitcnt vmcnt(15)
	v_pk_mul_f32 v[196:197], v[196:197], s[16:17] op_sel_hi:[1,0]
	v_pk_mul_f32 v[194:195], v[194:195], s[16:17] op_sel_hi:[1,0]
	v_pk_fma_f32 v[196:197], v[92:93], v[12:13], v[196:197]
	v_pk_fma_f32 v[194:195], v[90:91], v[10:11], v[194:195]
	s_nop 0
	v_cvt_pk_bf16_f32 v194, v194, v195
	v_cvt_pk_bf16_f32 v195, v196, v197
	global_store_dwordx2 v[24:25], v[194:195], off offset:32
	s_waitcnt vmcnt(15)
	v_pk_mul_f32 v[200:201], v[200:201], s[16:17] op_sel_hi:[1,0]
	v_pk_mul_f32 v[198:199], v[198:199], s[16:17] op_sel_hi:[1,0]
	v_pk_fma_f32 v[200:201], v[88:89], v[8:9], v[200:201]
	v_pk_fma_f32 v[198:199], v[86:87], v[6:7], v[198:199]
	s_nop 0
	v_cvt_pk_bf16_f32 v198, v198, v199
	v_cvt_pk_bf16_f32 v199, v200, v201
	global_store_dwordx2 v[24:25], v[198:199], off offset:256
	v_lshl_add_u64 v[28:29], v[26:27], 2, s[36:37]
	s_waitcnt vmcnt(15)
	v_pk_mul_f32 v[204:205], v[204:205], s[16:17] op_sel_hi:[1,0]
	v_pk_mul_f32 v[202:203], v[202:203], s[16:17] op_sel_hi:[1,0]
	v_pk_fma_f32 v[204:205], v[80:81], v[4:5], v[204:205]
	v_pk_fma_f32 v[202:203], v[78:79], v[2:3], v[202:203]
	s_nop 0
	v_cvt_pk_bf16_f32 v202, v202, v203
	v_cvt_pk_bf16_f32 v203, v204, v205
	global_store_dwordx2 v[24:25], v[202:203], off offset:288
	v_lshl_add_u64 v[24:25], v[26:27], 1, s[8:9]
	v_lshl_add_u64 v[26:27], v[18:19], 0, s[20:21]
	s_waitcnt vmcnt(15)
	v_pk_mul_f32 v[208:209], v[208:209], s[16:17] op_sel_hi:[1,0]
	v_pk_mul_f32 v[206:207], v[206:207], s[16:17] op_sel_hi:[1,0]
	v_pk_fma_f32 v[208:209], v[84:85], v[16:17], v[208:209]
	v_pk_fma_f32 v[206:207], v[82:83], v[14:15], v[206:207]
	s_nop 0
	v_cvt_pk_bf16_f32 v206, v206, v207
	v_cvt_pk_bf16_f32 v207, v208, v209
	global_store_dwordx2 v[24:25], v[206:207], off
	s_waitcnt vmcnt(15)
	v_pk_mul_f32 v[212:213], v[212:213], s[16:17] op_sel_hi:[1,0]
	v_pk_mul_f32 v[210:211], v[210:211], s[16:17] op_sel_hi:[1,0]
	v_pk_fma_f32 v[212:213], v[76:77], v[12:13], v[212:213]
	v_pk_fma_f32 v[210:211], v[74:75], v[10:11], v[210:211]
	s_nop 0
	v_cvt_pk_bf16_f32 v210, v210, v211
	v_cvt_pk_bf16_f32 v211, v212, v213
	global_store_dwordx2 v[24:25], v[210:211], off offset:32
	s_waitcnt vmcnt(15)
	v_pk_mul_f32 v[216:217], v[216:217], s[16:17] op_sel_hi:[1,0]
	v_pk_mul_f32 v[214:215], v[214:215], s[16:17] op_sel_hi:[1,0]
	v_pk_fma_f32 v[216:217], v[72:73], v[8:9], v[216:217]
	v_pk_fma_f32 v[214:215], v[70:71], v[6:7], v[214:215]
	s_nop 0
	v_cvt_pk_bf16_f32 v214, v214, v215
	v_cvt_pk_bf16_f32 v215, v216, v217
	global_store_dwordx2 v[24:25], v[214:215], off offset:256
	v_lshl_add_u64 v[28:29], v[26:27], 2, s[36:37]
	s_waitcnt vmcnt(15)
	v_pk_mul_f32 v[220:221], v[220:221], s[16:17] op_sel_hi:[1,0]
	v_pk_mul_f32 v[218:219], v[218:219], s[16:17] op_sel_hi:[1,0]
	v_pk_fma_f32 v[220:221], v[64:65], v[4:5], v[220:221]
	v_pk_fma_f32 v[218:219], v[62:63], v[2:3], v[218:219]
	s_nop 0
	v_cvt_pk_bf16_f32 v218, v218, v219
	v_cvt_pk_bf16_f32 v219, v220, v221
	global_store_dwordx2 v[24:25], v[218:219], off offset:288
	v_lshl_add_u64 v[24:25], v[26:27], 1, s[8:9]
	v_lshl_add_u64 v[26:27], v[18:19], 0, s[22:23]
	s_waitcnt vmcnt(15)
	v_pk_mul_f32 v[224:225], v[224:225], s[16:17] op_sel_hi:[1,0]
	v_pk_mul_f32 v[222:223], v[222:223], s[16:17] op_sel_hi:[1,0]
	v_pk_fma_f32 v[224:225], v[68:69], v[16:17], v[224:225]
	v_pk_fma_f32 v[222:223], v[66:67], v[14:15], v[222:223]
	s_nop 0
	v_cvt_pk_bf16_f32 v222, v222, v223
	v_cvt_pk_bf16_f32 v223, v224, v225
	global_store_dwordx2 v[24:25], v[222:223], off
	s_waitcnt vmcnt(15)
	v_pk_mul_f32 v[228:229], v[228:229], s[16:17] op_sel_hi:[1,0]
	v_pk_mul_f32 v[226:227], v[226:227], s[16:17] op_sel_hi:[1,0]
	v_pk_fma_f32 v[228:229], v[60:61], v[12:13], v[228:229]
	v_pk_fma_f32 v[226:227], v[58:59], v[10:11], v[226:227]
	s_nop 0
	v_cvt_pk_bf16_f32 v226, v226, v227
	v_cvt_pk_bf16_f32 v227, v228, v229
	global_store_dwordx2 v[24:25], v[226:227], off offset:32
	s_waitcnt vmcnt(15)
	v_pk_mul_f32 v[232:233], v[232:233], s[16:17] op_sel_hi:[1,0]
	v_pk_mul_f32 v[230:231], v[230:231], s[16:17] op_sel_hi:[1,0]
	v_pk_fma_f32 v[232:233], v[56:57], v[8:9], v[232:233]
	v_pk_fma_f32 v[230:231], v[54:55], v[6:7], v[230:231]
	s_nop 0
	v_cvt_pk_bf16_f32 v230, v230, v231
	v_cvt_pk_bf16_f32 v231, v232, v233
	global_store_dwordx2 v[24:25], v[230:231], off offset:256
	v_lshl_add_u64 v[28:29], v[26:27], 2, s[36:37]
	s_waitcnt vmcnt(15)
	v_pk_mul_f32 v[18:19], v[236:237], s[16:17] op_sel_hi:[1,0]
	v_pk_mul_f32 v[234:235], v[234:235], s[16:17] op_sel_hi:[1,0]
	v_pk_fma_f32 v[18:19], v[48:49], v[4:5], v[18:19]
	v_pk_fma_f32 v[234:235], v[46:47], v[2:3], v[234:235]
	v_lshl_add_u64 v[22:23], v[26:27], 1, s[8:9]
	v_cvt_pk_bf16_f32 v234, v234, v235
	v_cvt_pk_bf16_f32 v235, v18, v19
	global_store_dwordx2 v[24:25], v[234:235], off offset:288
	s_waitcnt vmcnt(15)
	v_pk_mul_f32 v[240:241], v[240:241], s[16:17] op_sel_hi:[1,0]
	v_pk_mul_f32 v[238:239], v[238:239], s[16:17] op_sel_hi:[1,0]
	v_pk_fma_f32 v[16:17], v[52:53], v[16:17], v[240:241]
	v_pk_fma_f32 v[14:15], v[50:51], v[14:15], v[238:239]
	s_nop 0
	v_cvt_pk_bf16_f32 v14, v14, v15
	v_cvt_pk_bf16_f32 v15, v16, v17
	global_store_dwordx2 v[22:23], v[14:15], off
	s_waitcnt vmcnt(15)
	v_pk_mul_f32 v[244:245], v[244:245], s[16:17] op_sel_hi:[1,0]
	v_pk_mul_f32 v[242:243], v[242:243], s[16:17] op_sel_hi:[1,0]
	v_pk_fma_f32 v[12:13], v[44:45], v[12:13], v[244:245]
	v_pk_fma_f32 v[10:11], v[42:43], v[10:11], v[242:243]
	s_nop 0
	v_cvt_pk_bf16_f32 v10, v10, v11
	v_cvt_pk_bf16_f32 v11, v12, v13
	global_store_dwordx2 v[22:23], v[10:11], off offset:32
	s_waitcnt vmcnt(15)
	v_pk_mul_f32 v[248:249], v[248:249], s[16:17] op_sel_hi:[1,0]
	v_pk_mul_f32 v[246:247], v[246:247], s[16:17] op_sel_hi:[1,0]
	v_pk_fma_f32 v[8:9], v[40:41], v[8:9], v[248:249]
	v_pk_fma_f32 v[6:7], v[38:39], v[6:7], v[246:247]
	s_nop 0
	v_cvt_pk_bf16_f32 v6, v6, v7
	v_cvt_pk_bf16_f32 v7, v8, v9
	global_store_dwordx2 v[22:23], v[6:7], off offset:256
	s_waitcnt vmcnt(15)
	v_pk_mul_f32 v[252:253], v[252:253], s[16:17] op_sel_hi:[1,0]
	v_pk_mul_f32 v[250:251], v[250:251], s[16:17] op_sel_hi:[1,0]
	v_pk_fma_f32 v[4:5], v[36:37], v[4:5], v[252:253]
	v_pk_fma_f32 v[2:3], v[34:35], v[2:3], v[250:251]
	s_nop 0
	v_cvt_pk_bf16_f32 v2, v2, v3
	v_cvt_pk_bf16_f32 v3, v4, v5
	global_store_dwordx2 v[22:23], v[2:3], off offset:288
	s_cbranch_vccnz .LBB0_2437
	s_andn2_b64 vcc, exec, s[6:7]
	s_cbranch_vccnz .LBB0_2436
	s_barrier
	s_branch .LBB0_2436

	.amdhsa_kernel _Z10hybrid_fwd4Args
		.amdhsa_group_segment_fixed_size 0
		.amdhsa_private_segment_fixed_size 0
		.amdhsa_kernarg_size 464
		.amdhsa_user_sgpr_count 2
		.amdhsa_user_sgpr_dispatch_ptr 0
		.amdhsa_user_sgpr_queue_ptr 0
		.amdhsa_user_sgpr_kernarg_segment_ptr 1
		.amdhsa_user_sgpr_dispatch_id 0
		.amdhsa_user_sgpr_kernarg_preload_length 0
		.amdhsa_user_sgpr_kernarg_preload_offset 0
		.amdhsa_user_sgpr_private_segment_size 0
		.amdhsa_uses_dynamic_stack 0
		.amdhsa_enable_private_segment 0
		.amdhsa_system_sgpr_workgroup_id_x 1
		.amdhsa_system_sgpr_workgroup_id_y 0
		.amdhsa_system_sgpr_workgroup_id_z 0
		.amdhsa_system_sgpr_workgroup_info 0
		.amdhsa_system_vgpr_workitem_id 0
		.amdhsa_next_free_vgpr 256
		.amdhsa_next_free_sgpr 100
		.amdhsa_accum_offset 256
		.amdhsa_reserve_vcc 1
		.amdhsa_float_round_mode_32 0
		.amdhsa_float_round_mode_16_64 0
		.amdhsa_float_denorm_mode_32 3
		.amdhsa_float_denorm_mode_16_64 3
		.amdhsa_dx10_clamp 1
		.amdhsa_ieee_mode 1
		.amdhsa_fp16_overflow 0
		.amdhsa_tg_split 0
		.amdhsa_exception_fp_ieee_invalid_op 0
		.amdhsa_exception_fp_denorm_src 0
		.amdhsa_exception_fp_ieee_div_zero 0
		.amdhsa_exception_fp_ieee_overflow 0
		.amdhsa_exception_fp_ieee_underflow 0
		.amdhsa_exception_fp_ieee_inexact 0
		.amdhsa_exception_int_div_zero 0
	.end_amdhsa_kernel

amdhsa.kernels:
  - .agpr_count:     0
    .args:
      - .offset:         0
        .size:           208
        .value_kind:     by_value
      - .offset:         208
        .size:           4
        .value_kind:     hidden_block_count_x
      - .offset:         212
        .size:           4
        .value_kind:     hidden_block_count_y
      - .offset:         216
        .size:           4
        .value_kind:     hidden_block_count_z
      - .offset:         220
        .size:           2
        .value_kind:     hidden_group_size_x
      - .offset:         222
        .size:           2
        .value_kind:     hidden_group_size_y
      - .offset:         224
        .size:           2
        .value_kind:     hidden_group_size_z
      - .offset:         226
        .size:           2
        .value_kind:     hidden_remainder_x
      - .offset:         228
        .size:           2
        .value_kind:     hidden_remainder_y
      - .offset:         230
        .size:           2
        .value_kind:     hidden_remainder_z
      - .offset:         248
        .size:           8
        .value_kind:     hidden_global_offset_x
      - .offset:         256
        .size:           8
        .value_kind:     hidden_global_offset_y
      - .offset:         264
        .size:           8
        .value_kind:     hidden_global_offset_z
      - .offset:         272
        .size:           2
        .value_kind:     hidden_grid_dims
      - .offset:         328
        .size:           4
        .value_kind:     hidden_dynamic_lds_size
    .group_segment_fixed_size: 0
    .kernarg_segment_align: 8
    .kernarg_segment_size: 464
    .language:       OpenCL C
    .language_version:
      - 2
      - 0
    .max_flat_workgroup_size: 512
    .name:           _Z10hybrid_fwd4Args
    .private_segment_fixed_size: 0
    .sgpr_count:     106
    .sgpr_spill_count: 78
    .symbol:         _Z10hybrid_fwd4Args.kd
    .uniform_work_group_size: 1
    .uses_dynamic_stack: false
    .vgpr_count:     256
    .vgpr_spill_count: 0
    .wavefront_size: 64
